# baseline (speedup 1.0000x reference)
.Lg1_noX:
	v_permlane16_swap_b32_e32 v158, v160
	v_permlane16_swap_b32_e32 v159, v161
	global_store_dwordx4 v228, v[158:161], s[58:59] offset:128 nt
	v_exp_f32_e32 v130, v90
	v_exp_f32_e32 v131, v91
	v_exp_f32_e32 v132, v92
	v_exp_f32_e32 v133, v93
	v_exp_f32_e32 v142, v42
	v_exp_f32_e32 v143, v43
	v_exp_f32_e32 v144, v44
	v_exp_f32_e32 v145, v45
	v_exp_f32_e32 v176, v126
	v_exp_f32_e32 v177, v127
	v_exp_f32_e32 v178, v128
	v_exp_f32_e32 v179, v129
	v_exp_f32_e32 v232, v58
	v_exp_f32_e32 v233, v59
	v_exp_f32_e32 v234, v60
	v_exp_f32_e32 v235, v61
	v_pk_fma_f32 v[130:131], v[130:131], -0.5, -0.5 op_sel_hi:[1,0,0]
	v_pk_fma_f32 v[132:133], v[132:133], -0.5, -0.5 op_sel_hi:[1,0,0]
	v_pk_fma_f32 v[142:143], v[142:143], -0.5, -0.5 op_sel_hi:[1,0,0]
	v_pk_fma_f32 v[144:145], v[144:145], -0.5, -0.5 op_sel_hi:[1,0,0]
	v_pk_fma_f32 v[176:177], v[176:177], -0.5, -0.5 op_sel_hi:[1,0,0]
	v_pk_fma_f32 v[178:179], v[178:179], -0.5, -0.5 op_sel_hi:[1,0,0]
	v_pk_fma_f32 v[232:233], v[232:233], -0.5, -0.5 op_sel_hi:[1,0,0]
	v_pk_fma_f32 v[234:235], v[234:235], -0.5, -0.5 op_sel_hi:[1,0,0]
	v_pk_mul_f32 v[134:135], v[130:131], v[132:133]
	v_pk_mul_f32 v[146:147], v[142:143], v[144:145]
	v_pk_mul_f32 v[180:181], v[176:177], v[178:179]
	v_pk_mul_f32 v[236:237], v[232:233], v[234:235]
	v_mul_f32_e32 v188, v134, v135
	v_mul_f32_e32 v190, v146, v147
	v_mul_f32_e32 v189, v180, v181
	v_mul_f32_e32 v191, v236, v237
	v_pk_mul_f32 v[192:193], v[188:189], v[190:191]
	v_mul_f32_e32 v174, v192, v193
	v_rcp_f32_e32 v173, v174
	v_pk_add_f32 v[164:165], v[164:165], v[90:91]
	v_pk_add_f32 v[164:165], v[164:165], v[92:93]
	v_pk_add_f32 v[164:165], v[164:165], v[42:43]
	v_pk_add_f32 v[164:165], v[164:165], v[44:45]
	v_pk_add_f32 v[164:165], v[164:165], v[126:127]
	v_pk_add_f32 v[164:165], v[164:165], v[128:129]
	v_pk_add_f32 v[164:165], v[164:165], v[58:59]
	v_pk_add_f32 v[164:165], v[164:165], v[60:61]
	v_pk_mul_f32 v[230:231], v[172:173], v[192:193] op_sel:[1,1] op_sel_hi:[1,0]
	v_pk_mul_f32 v[192:193], v[230:231], v[190:191]
	v_pk_mul_f32 v[190:191], v[230:231], v[188:189]
	v_pk_mul_f32 v[136:137], v[192:193], v[134:135] op_sel:[0,1] op_sel_hi:[0,0]
	v_pk_mul_f32 v[148:149], v[190:191], v[146:147] op_sel:[0,1] op_sel_hi:[0,0]
	v_pk_mul_f32 v[182:183], v[192:193], v[180:181] op_sel:[1,1] op_sel_hi:[1,0]
	v_pk_mul_f32 v[238:239], v[190:191], v[236:237] op_sel:[1,1] op_sel_hi:[1,0]
	v_pk_fma_f32 v[138:139], v[136:137], v[132:133], 1.0 op_sel_hi:[1,1,0]
	v_pk_fma_f32 v[140:141], v[136:137], v[130:131], 1.0 op_sel_hi:[1,1,0]
	v_pk_fma_f32 v[150:151], v[148:149], v[144:145], 1.0 op_sel_hi:[1,1,0]
	v_pk_fma_f32 v[152:153], v[148:149], v[142:143], 1.0 op_sel_hi:[1,1,0]
	v_pk_fma_f32 v[184:185], v[182:183], v[178:179], 1.0 op_sel_hi:[1,1,0]
	v_pk_fma_f32 v[186:187], v[182:183], v[176:177], 1.0 op_sel_hi:[1,1,0]
	v_pk_fma_f32 v[240:241], v[238:239], v[234:235], 1.0 op_sel_hi:[1,1,0]
	v_pk_fma_f32 v[242:243], v[238:239], v[232:233], 1.0 op_sel_hi:[1,1,0]
	v_cvt_pk_bf16_f32 v154, v138, v139
	v_cvt_pk_bf16_f32 v155, v140, v141
	v_cvt_pk_bf16_f32 v156, v150, v151
	v_cvt_pk_bf16_f32 v157, v152, v153
	v_cvt_pk_bf16_f32 v158, v184, v185
	v_cvt_pk_bf16_f32 v159, v186, v187
	v_cvt_pk_bf16_f32 v160, v240, v241
	v_cvt_pk_bf16_f32 v161, v242, v243
	ds_read_b128 v[90:93], v172 offset:512
	ds_read_b128 v[42:45], v172 offset:576
	ds_read_b128 v[126:129], v172 offset:640
	ds_read_b128 v[58:61], v172 offset:704
	v_permlane16_swap_b32_e32 v154, v156
	v_permlane16_swap_b32_e32 v155, v157
	global_store_dwordx4 v228, v[154:157], s[62:63] nt
	v_permlane16_swap_b32_e32 v158, v160
	v_permlane16_swap_b32_e32 v159, v161
	global_store_dwordx4 v228, v[158:161], s[62:63] offset:128 nt
	v_mul_f32_e32 v166, v162, v174
	v_log_f32_e32 v166, v166
	v_add_f32_e32 v168, v164, v165
	v_mul_f32_e32 v168, 0xbeb17218, v168
	v_fmac_f32_e32 v168, 0x3f317218, v166
	v_mov_b32_e32 v169, v168
	s_nop 1
	v_permlane16_swap_b32_e32 v168, v169
	v_add_f32_e32 v168, v168, v169
	v_mov_b32_e32 v169, v168
	s_nop 1
	v_permlane32_swap_b32_e32 v168, v169
	v_add_f32_e32 v168, v168, v169
	s_mov_b64 exec, s[0:1]
	global_store_dword v229, v168, s[66:67]
	s_mov_b64 exec, -1
	v_exp_f32_e32 v130, v110
	v_exp_f32_e32 v131, v111
	v_exp_f32_e32 v132, v112
	v_exp_f32_e32 v133, v113
	v_exp_f32_e32 v142, v74
	v_exp_f32_e32 v143, v75
	v_exp_f32_e32 v144, v76
	v_exp_f32_e32 v145, v77
	v_exp_f32_e32 v176, v102
	v_exp_f32_e32 v177, v103
	v_exp_f32_e32 v178, v104
	v_exp_f32_e32 v179, v105
	v_exp_f32_e32 v232, v66
	v_exp_f32_e32 v233, v67
	v_exp_f32_e32 v234, v68
	v_exp_f32_e32 v235, v69
	v_pk_fma_f32 v[130:131], v[130:131], -0.5, -0.5 op_sel_hi:[1,0,0]
	v_pk_fma_f32 v[132:133], v[132:133], -0.5, -0.5 op_sel_hi:[1,0,0]
	v_pk_fma_f32 v[142:143], v[142:143], -0.5, -0.5 op_sel_hi:[1,0,0]
	v_pk_fma_f32 v[144:145], v[144:145], -0.5, -0.5 op_sel_hi:[1,0,0]
	v_pk_fma_f32 v[176:177], v[176:177], -0.5, -0.5 op_sel_hi:[1,0,0]
	v_pk_fma_f32 v[178:179], v[178:179], -0.5, -0.5 op_sel_hi:[1,0,0]
	v_pk_fma_f32 v[232:233], v[232:233], -0.5, -0.5 op_sel_hi:[1,0,0]
	v_pk_fma_f32 v[234:235], v[234:235], -0.5, -0.5 op_sel_hi:[1,0,0]
	v_pk_mul_f32 v[134:135], v[130:131], v[132:133]
	v_pk_mul_f32 v[146:147], v[142:143], v[144:145]
	v_pk_mul_f32 v[180:181], v[176:177], v[178:179]
	v_pk_mul_f32 v[236:237], v[232:233], v[234:235]
	v_mul_f32_e32 v188, v134, v135
	v_mul_f32_e32 v190, v146, v147
	v_mul_f32_e32 v189, v180, v181
	v_mul_f32_e32 v191, v236, v237
	v_pk_mul_f32 v[192:193], v[188:189], v[190:191]
	v_mul_f32_e32 v162, v192, v193
	v_rcp_f32_e32 v173, v162
	v_pk_add_f32 v[164:165], v[110:111], v[112:113]
	v_pk_add_f32 v[164:165], v[164:165], v[74:75]
	v_pk_add_f32 v[164:165], v[164:165], v[76:77]
	v_pk_add_f32 v[164:165], v[164:165], v[102:103]
	v_pk_add_f32 v[164:165], v[164:165], v[104:105]
	v_pk_add_f32 v[164:165], v[164:165], v[66:67]
	v_pk_add_f32 v[164:165], v[164:165], v[68:69]
	v_pk_mul_f32 v[230:231], v[172:173], v[192:193] op_sel:[1,1] op_sel_hi:[1,0]
	v_pk_mul_f32 v[192:193], v[230:231], v[190:191]
	v_pk_mul_f32 v[190:191], v[230:231], v[188:189]
	v_pk_mul_f32 v[136:137], v[192:193], v[134:135] op_sel:[0,1] op_sel_hi:[0,0]
	v_pk_mul_f32 v[148:149], v[190:191], v[146:147] op_sel:[0,1] op_sel_hi:[0,0]
	v_pk_mul_f32 v[182:183], v[192:193], v[180:181] op_sel:[1,1] op_sel_hi:[1,0]
	v_pk_mul_f32 v[238:239], v[190:191], v[236:237] op_sel:[1,1] op_sel_hi:[1,0]
	v_pk_fma_f32 v[138:139], v[136:137], v[132:133], 1.0 op_sel_hi:[1,1,0]
	v_pk_fma_f32 v[140:141], v[136:137], v[130:131], 1.0 op_sel_hi:[1,1,0]
	v_pk_fma_f32 v[150:151], v[148:149], v[144:145], 1.0 op_sel_hi:[1,1,0]
	v_pk_fma_f32 v[152:153], v[148:149], v[142:143], 1.0 op_sel_hi:[1,1,0]
	v_pk_fma_f32 v[184:185], v[182:183], v[178:179], 1.0 op_sel_hi:[1,1,0]
	v_pk_fma_f32 v[186:187], v[182:183], v[176:177], 1.0 op_sel_hi:[1,1,0]
	v_pk_fma_f32 v[240:241], v[238:239], v[234:235], 1.0 op_sel_hi:[1,1,0]
	v_pk_fma_f32 v[242:243], v[238:239], v[232:233], 1.0 op_sel_hi:[1,1,0]
	v_cvt_pk_bf16_f32 v154, v138, v139
	v_cvt_pk_bf16_f32 v155, v140, v141
	v_cvt_pk_bf16_f32 v156, v150, v151
	v_cvt_pk_bf16_f32 v157, v152, v153
	v_cvt_pk_bf16_f32 v158, v184, v185
	v_cvt_pk_bf16_f32 v159, v186, v187
	v_cvt_pk_bf16_f32 v160, v240, v241
	v_cvt_pk_bf16_f32 v161, v242, v243
	ds_read_b128 v[110:113], v172
	ds_read_b128 v[74:77], v172 offset:64
	ds_read_b128 v[102:105], v172 offset:128
	ds_read_b128 v[66:69], v172 offset:192
	v_permlane16_swap_b32_e32 v154, v156
	v_permlane16_swap_b32_e32 v155, v157
	global_store_dwordx4 v228, v[154:157], s[58:59] offset:2048 nt
	v_permlane16_swap_b32_e32 v158, v160
	v_permlane16_swap_b32_e32 v159, v161
	global_store_dwordx4 v228, v[158:161], s[58:59] offset:2176 nt
	v_exp_f32_e32 v130, v86
	v_exp_f32_e32 v131, v87
	v_exp_f32_e32 v132, v88
	v_exp_f32_e32 v133, v89
	v_exp_f32_e32 v142, v38
	v_exp_f32_e32 v143, v39
	v_exp_f32_e32 v144, v40
	v_exp_f32_e32 v145, v41
	v_exp_f32_e32 v176, v122
	v_exp_f32_e32 v177, v123
	v_exp_f32_e32 v178, v124
	v_exp_f32_e32 v179, v125
	v_exp_f32_e32 v232, v50
	v_exp_f32_e32 v233, v51
	v_exp_f32_e32 v234, v52
	v_exp_f32_e32 v235, v53
	v_pk_fma_f32 v[130:131], v[130:131], -0.5, -0.5 op_sel_hi:[1,0,0]
	v_pk_fma_f32 v[132:133], v[132:133], -0.5, -0.5 op_sel_hi:[1,0,0]
	v_pk_fma_f32 v[142:143], v[142:143], -0.5, -0.5 op_sel_hi:[1,0,0]
	v_pk_fma_f32 v[144:145], v[144:145], -0.5, -0.5 op_sel_hi:[1,0,0]
	v_pk_fma_f32 v[176:177], v[176:177], -0.5, -0.5 op_sel_hi:[1,0,0]
	v_pk_fma_f32 v[178:179], v[178:179], -0.5, -0.5 op_sel_hi:[1,0,0]
	v_pk_fma_f32 v[232:233], v[232:233], -0.5, -0.5 op_sel_hi:[1,0,0]
	v_pk_fma_f32 v[234:235], v[234:235], -0.5, -0.5 op_sel_hi:[1,0,0]
	v_pk_mul_f32 v[134:135], v[130:131], v[132:133]
	v_pk_mul_f32 v[146:147], v[142:143], v[144:145]
	v_pk_mul_f32 v[180:181], v[176:177], v[178:179]
	v_pk_mul_f32 v[236:237], v[232:233], v[234:235]
	v_mul_f32_e32 v188, v134, v135
	v_mul_f32_e32 v190, v146, v147
	v_mul_f32_e32 v189, v180, v181
	v_mul_f32_e32 v191, v236, v237
	v_pk_mul_f32 v[192:193], v[188:189], v[190:191]
	v_mul_f32_e32 v174, v192, v193
	v_rcp_f32_e32 v173, v174
	v_pk_add_f32 v[164:165], v[164:165], v[86:87]
	v_pk_add_f32 v[164:165], v[164:165], v[88:89]
	v_pk_add_f32 v[164:165], v[164:165], v[38:39]
	v_pk_add_f32 v[164:165], v[164:165], v[40:41]
	v_pk_add_f32 v[164:165], v[164:165], v[122:123]
	v_pk_add_f32 v[164:165], v[164:165], v[124:125]
	v_pk_add_f32 v[164:165], v[164:165], v[50:51]
	v_pk_add_f32 v[164:165], v[164:165], v[52:53]
	v_pk_mul_f32 v[230:231], v[172:173], v[192:193] op_sel:[1,1] op_sel_hi:[1,0]
	v_pk_mul_f32 v[192:193], v[230:231], v[190:191]
	v_pk_mul_f32 v[190:191], v[230:231], v[188:189]
	v_pk_mul_f32 v[136:137], v[192:193], v[134:135] op_sel:[0,1] op_sel_hi:[0,0]
	v_pk_mul_f32 v[148:149], v[190:191], v[146:147] op_sel:[0,1] op_sel_hi:[0,0]
	v_pk_mul_f32 v[182:183], v[192:193], v[180:181] op_sel:[1,1] op_sel_hi:[1,0]
	v_pk_mul_f32 v[238:239], v[190:191], v[236:237] op_sel:[1,1] op_sel_hi:[1,0]
	v_pk_fma_f32 v[138:139], v[136:137], v[132:133], 1.0 op_sel_hi:[1,1,0]
	v_pk_fma_f32 v[140:141], v[136:137], v[130:131], 1.0 op_sel_hi:[1,1,0]
	v_pk_fma_f32 v[150:151], v[148:149], v[144:145], 1.0 op_sel_hi:[1,1,0]
	v_pk_fma_f32 v[152:153], v[148:149], v[142:143], 1.0 op_sel_hi:[1,1,0]
	v_pk_fma_f32 v[184:185], v[182:183], v[178:179], 1.0 op_sel_hi:[1,1,0]
	v_pk_fma_f32 v[186:187], v[182:183], v[176:177], 1.0 op_sel_hi:[1,1,0]
	v_pk_fma_f32 v[240:241], v[238:239], v[234:235], 1.0 op_sel_hi:[1,1,0]
	v_pk_fma_f32 v[242:243], v[238:239], v[232:233], 1.0 op_sel_hi:[1,1,0]
	v_cvt_pk_bf16_f32 v154, v138, v139
	v_cvt_pk_bf16_f32 v155, v140, v141
	v_cvt_pk_bf16_f32 v156, v150, v151
	v_cvt_pk_bf16_f32 v157, v152, v153
	v_cvt_pk_bf16_f32 v158, v184, v185
	v_cvt_pk_bf16_f32 v159, v186, v187
	v_cvt_pk_bf16_f32 v160, v240, v241
	v_cvt_pk_bf16_f32 v161, v242, v243
	ds_read_b128 v[86:89], v172 offset:512
	ds_read_b128 v[38:41], v172 offset:576
	ds_read_b128 v[122:125], v172 offset:640
	ds_read_b128 v[50:53], v172 offset:704
	v_permlane16_swap_b32_e32 v154, v156
	v_permlane16_swap_b32_e32 v155, v157
	global_store_dwordx4 v228, v[154:157], s[62:63] offset:2048 nt
	v_permlane16_swap_b32_e32 v158, v160
	v_permlane16_swap_b32_e32 v159, v161
	global_store_dwordx4 v228, v[158:161], s[62:63] offset:2176 nt
	v_mul_f32_e32 v166, v162, v174
	v_log_f32_e32 v166, v166
	v_add_f32_e32 v168, v164, v165
	v_mul_f32_e32 v168, 0xbeb17218, v168
	v_fmac_f32_e32 v168, 0x3f317218, v166
	v_mov_b32_e32 v169, v168
	s_nop 1
	v_permlane16_swap_b32_e32 v168, v169
	v_add_f32_e32 v168, v168, v169
	v_mov_b32_e32 v169, v168
	s_nop 1
	v_permlane32_swap_b32_e32 v168, v169
	v_add_f32_e32 v168, v168, v169
	s_mov_b64 exec, s[0:1]
	global_store_dword v229, v168, s[66:67] offset:64
	s_mov_b64 exec, -1
	v_exp_f32_e32 v130, v98
	v_exp_f32_e32 v131, v99
	v_exp_f32_e32 v132, v100
	v_exp_f32_e32 v133, v101
	v_exp_f32_e32 v142, v62
	v_exp_f32_e32 v143, v63
	v_exp_f32_e32 v144, v64
	v_exp_f32_e32 v145, v65
	v_exp_f32_e32 v176, v94
	v_exp_f32_e32 v177, v95
	v_exp_f32_e32 v178, v96
	v_exp_f32_e32 v179, v97
	v_exp_f32_e32 v232, v54
	v_exp_f32_e32 v233, v55
	v_exp_f32_e32 v234, v56
	v_exp_f32_e32 v235, v57
	v_pk_fma_f32 v[130:131], v[130:131], -0.5, -0.5 op_sel_hi:[1,0,0]
	v_pk_fma_f32 v[132:133], v[132:133], -0.5, -0.5 op_sel_hi:[1,0,0]
	v_pk_fma_f32 v[142:143], v[142:143], -0.5, -0.5 op_sel_hi:[1,0,0]
	v_pk_fma_f32 v[144:145], v[144:145], -0.5, -0.5 op_sel_hi:[1,0,0]
	v_pk_fma_f32 v[176:177], v[176:177], -0.5, -0.5 op_sel_hi:[1,0,0]
	v_pk_fma_f32 v[178:179], v[178:179], -0.5, -0.5 op_sel_hi:[1,0,0]
	v_pk_fma_f32 v[232:233], v[232:233], -0.5, -0.5 op_sel_hi:[1,0,0]
	v_pk_fma_f32 v[234:235], v[234:235], -0.5, -0.5 op_sel_hi:[1,0,0]
	v_pk_mul_f32 v[134:135], v[130:131], v[132:133]
	v_pk_mul_f32 v[146:147], v[142:143], v[144:145]
	v_pk_mul_f32 v[180:181], v[176:177], v[178:179]
	v_pk_mul_f32 v[236:237], v[232:233], v[234:235]
	v_mul_f32_e32 v188, v134, v135
	v_mul_f32_e32 v190, v146, v147
	v_mul_f32_e32 v189, v180, v181
	v_mul_f32_e32 v191, v236, v237
	v_pk_mul_f32 v[192:193], v[188:189], v[190:191]
	v_mul_f32_e32 v162, v192, v193
	v_rcp_f32_e32 v173, v162
	v_pk_add_f32 v[164:165], v[98:99], v[100:101]
	v_pk_add_f32 v[164:165], v[164:165], v[62:63]
	v_pk_add_f32 v[164:165], v[164:165], v[64:65]
	v_pk_add_f32 v[164:165], v[164:165], v[94:95]
	v_pk_add_f32 v[164:165], v[164:165], v[96:97]
	v_pk_add_f32 v[164:165], v[164:165], v[54:55]
	v_pk_add_f32 v[164:165], v[164:165], v[56:57]
	v_pk_mul_f32 v[230:231], v[172:173], v[192:193] op_sel:[1,1] op_sel_hi:[1,0]
	v_pk_mul_f32 v[192:193], v[230:231], v[190:191]
	v_pk_mul_f32 v[190:191], v[230:231], v[188:189]
	v_pk_mul_f32 v[136:137], v[192:193], v[134:135] op_sel:[0,1] op_sel_hi:[0,0]
	v_pk_mul_f32 v[148:149], v[190:191], v[146:147] op_sel:[0,1] op_sel_hi:[0,0]
	v_pk_mul_f32 v[182:183], v[192:193], v[180:181] op_sel:[1,1] op_sel_hi:[1,0]
	v_pk_mul_f32 v[238:239], v[190:191], v[236:237] op_sel:[1,1] op_sel_hi:[1,0]
	v_pk_fma_f32 v[138:139], v[136:137], v[132:133], 1.0 op_sel_hi:[1,1,0]
	v_pk_fma_f32 v[140:141], v[136:137], v[130:131], 1.0 op_sel_hi:[1,1,0]
	v_pk_fma_f32 v[150:151], v[148:149], v[144:145], 1.0 op_sel_hi:[1,1,0]
	v_pk_fma_f32 v[152:153], v[148:149], v[142:143], 1.0 op_sel_hi:[1,1,0]
	v_pk_fma_f32 v[184:185], v[182:183], v[178:179], 1.0 op_sel_hi:[1,1,0]
	v_pk_fma_f32 v[186:187], v[182:183], v[176:177], 1.0 op_sel_hi:[1,1,0]
	v_pk_fma_f32 v[240:241], v[238:239], v[234:235], 1.0 op_sel_hi:[1,1,0]
	v_pk_fma_f32 v[242:243], v[238:239], v[232:233], 1.0 op_sel_hi:[1,1,0]
	v_cvt_pk_bf16_f32 v154, v138, v139
	v_cvt_pk_bf16_f32 v155, v140, v141
	v_cvt_pk_bf16_f32 v156, v150, v151
	v_cvt_pk_bf16_f32 v157, v152, v153
	v_cvt_pk_bf16_f32 v158, v184, v185
	v_cvt_pk_bf16_f32 v159, v186, v187
	v_cvt_pk_bf16_f32 v160, v240, v241
	v_cvt_pk_bf16_f32 v161, v242, v243
	ds_read_b128 v[98:101], v172
	ds_read_b128 v[62:65], v172 offset:64
	ds_read_b128 v[94:97], v172 offset:128
	ds_read_b128 v[54:57], v172 offset:192
	v_permlane16_swap_b32_e32 v154, v156
	v_permlane16_swap_b32_e32 v155, v157
	global_store_dwordx4 v228, v[154:157], s[60:61] nt
	v_permlane16_swap_b32_e32 v158, v160
	v_permlane16_swap_b32_e32 v159, v161
	global_store_dwordx4 v228, v[158:161], s[60:61] offset:128 nt
	v_exp_f32_e32 v130, v82
	v_exp_f32_e32 v131, v83
	v_exp_f32_e32 v132, v84
	v_exp_f32_e32 v133, v85
	v_exp_f32_e32 v142, v34
	v_exp_f32_e32 v143, v35
	v_exp_f32_e32 v144, v36
	v_exp_f32_e32 v145, v37
	v_exp_f32_e32 v176, v118
	v_exp_f32_e32 v177, v119
	v_exp_f32_e32 v178, v120
	v_exp_f32_e32 v179, v121
	v_exp_f32_e32 v232, v46
	v_exp_f32_e32 v233, v47
	v_exp_f32_e32 v234, v48
	v_exp_f32_e32 v235, v49
	v_pk_fma_f32 v[130:131], v[130:131], -0.5, -0.5 op_sel_hi:[1,0,0]
	v_pk_fma_f32 v[132:133], v[132:133], -0.5, -0.5 op_sel_hi:[1,0,0]
	v_pk_fma_f32 v[142:143], v[142:143], -0.5, -0.5 op_sel_hi:[1,0,0]
	v_pk_fma_f32 v[144:145], v[144:145], -0.5, -0.5 op_sel_hi:[1,0,0]
	v_pk_fma_f32 v[176:177], v[176:177], -0.5, -0.5 op_sel_hi:[1,0,0]
	v_pk_fma_f32 v[178:179], v[178:179], -0.5, -0.5 op_sel_hi:[1,0,0]
	v_pk_fma_f32 v[232:233], v[232:233], -0.5, -0.5 op_sel_hi:[1,0,0]
	v_pk_fma_f32 v[234:235], v[234:235], -0.5, -0.5 op_sel_hi:[1,0,0]
	v_pk_mul_f32 v[134:135], v[130:131], v[132:133]
	v_pk_mul_f32 v[146:147], v[142:143], v[144:145]
	v_pk_mul_f32 v[180:181], v[176:177], v[178:179]
	v_pk_mul_f32 v[236:237], v[232:233], v[234:235]
	v_mul_f32_e32 v188, v134, v135
	v_mul_f32_e32 v190, v146, v147
	v_mul_f32_e32 v189, v180, v181
	v_mul_f32_e32 v191, v236, v237
	v_pk_mul_f32 v[192:193], v[188:189], v[190:191]
	v_mul_f32_e32 v174, v192, v193
	v_rcp_f32_e32 v173, v174
	v_pk_add_f32 v[164:165], v[164:165], v[82:83]
	v_pk_add_f32 v[164:165], v[164:165], v[84:85]
	v_pk_add_f32 v[164:165], v[164:165], v[34:35]
	v_pk_add_f32 v[164:165], v[164:165], v[36:37]
	v_pk_add_f32 v[164:165], v[164:165], v[118:119]
	v_pk_add_f32 v[164:165], v[164:165], v[120:121]
	v_pk_add_f32 v[164:165], v[164:165], v[46:47]
	v_pk_add_f32 v[164:165], v[164:165], v[48:49]
	v_pk_mul_f32 v[230:231], v[172:173], v[192:193] op_sel:[1,1] op_sel_hi:[1,0]
	v_pk_mul_f32 v[192:193], v[230:231], v[190:191]
	v_pk_mul_f32 v[190:191], v[230:231], v[188:189]
	v_pk_mul_f32 v[136:137], v[192:193], v[134:135] op_sel:[0,1] op_sel_hi:[0,0]
	v_pk_mul_f32 v[148:149], v[190:191], v[146:147] op_sel:[0,1] op_sel_hi:[0,0]
	v_pk_mul_f32 v[182:183], v[192:193], v[180:181] op_sel:[1,1] op_sel_hi:[1,0]
	v_pk_mul_f32 v[238:239], v[190:191], v[236:237] op_sel:[1,1] op_sel_hi:[1,0]
	v_pk_fma_f32 v[138:139], v[136:137], v[132:133], 1.0 op_sel_hi:[1,1,0]
	v_pk_fma_f32 v[140:141], v[136:137], v[130:131], 1.0 op_sel_hi:[1,1,0]
	v_pk_fma_f32 v[150:151], v[148:149], v[144:145], 1.0 op_sel_hi:[1,1,0]
	v_pk_fma_f32 v[152:153], v[148:149], v[142:143], 1.0 op_sel_hi:[1,1,0]
	v_pk_fma_f32 v[184:185], v[182:183], v[178:179], 1.0 op_sel_hi:[1,1,0]
	v_pk_fma_f32 v[186:187], v[182:183], v[176:177], 1.0 op_sel_hi:[1,1,0]
	v_pk_fma_f32 v[240:241], v[238:239], v[234:235], 1.0 op_sel_hi:[1,1,0]
	v_pk_fma_f32 v[242:243], v[238:239], v[232:233], 1.0 op_sel_hi:[1,1,0]
	v_cvt_pk_bf16_f32 v154, v138, v139
	v_cvt_pk_bf16_f32 v155, v140, v141
	v_cvt_pk_bf16_f32 v156, v150, v151
	v_cvt_pk_bf16_f32 v157, v152, v153
	v_cvt_pk_bf16_f32 v158, v184, v185
	v_cvt_pk_bf16_f32 v159, v186, v187
	v_cvt_pk_bf16_f32 v160, v240, v241
	v_cvt_pk_bf16_f32 v161, v242, v243
	ds_read_b128 v[82:85], v172 offset:512
	ds_read_b128 v[34:37], v172 offset:576
	ds_read_b128 v[118:121], v172 offset:640
	ds_read_b128 v[46:49], v172 offset:704
	v_permlane16_swap_b32_e32 v154, v156
	v_permlane16_swap_b32_e32 v155, v157
	global_store_dwordx4 v228, v[154:157], s[64:65] nt
	v_permlane16_swap_b32_e32 v158, v160
	v_permlane16_swap_b32_e32 v159, v161
	global_store_dwordx4 v228, v[158:161], s[64:65] offset:128 nt
	v_mul_f32_e32 v166, v162, v174
	v_log_f32_e32 v166, v166
	v_add_f32_e32 v168, v164, v165
	v_mul_f32_e32 v168, 0xbeb17218, v168
	v_fmac_f32_e32 v168, 0x3f317218, v166
	v_mov_b32_e32 v169, v168
	s_nop 1
	v_permlane16_swap_b32_e32 v168, v169
	v_add_f32_e32 v168, v168, v169
	v_mov_b32_e32 v169, v168
	s_nop 1
	v_permlane32_swap_b32_e32 v168, v169
	v_add_f32_e32 v168, v168, v169
	s_mov_b64 exec, s[0:1]
	global_store_dword v229, v168, s[66:67] offset:512
	s_mov_b64 exec, -1
	v_exp_f32_e32 v130, v18
	v_exp_f32_e32 v131, v19
	v_exp_f32_e32 v132, v20
	v_exp_f32_e32 v133, v21
	v_exp_f32_e32 v142, v2
	v_exp_f32_e32 v143, v3
	v_exp_f32_e32 v144, v4
	v_exp_f32_e32 v145, v5
	v_exp_f32_e32 v176, v26
	v_exp_f32_e32 v177, v27
	v_exp_f32_e32 v178, v28
	v_exp_f32_e32 v179, v29
	v_exp_f32_e32 v232, v10
	v_exp_f32_e32 v233, v11
	v_exp_f32_e32 v234, v12
	v_exp_f32_e32 v235, v13
	v_pk_fma_f32 v[130:131], v[130:131], -0.5, -0.5 op_sel_hi:[1,0,0]
	v_pk_fma_f32 v[132:133], v[132:133], -0.5, -0.5 op_sel_hi:[1,0,0]
	v_pk_fma_f32 v[142:143], v[142:143], -0.5, -0.5 op_sel_hi:[1,0,0]
	v_pk_fma_f32 v[144:145], v[144:145], -0.5, -0.5 op_sel_hi:[1,0,0]
	v_pk_fma_f32 v[176:177], v[176:177], -0.5, -0.5 op_sel_hi:[1,0,0]
	v_pk_fma_f32 v[178:179], v[178:179], -0.5, -0.5 op_sel_hi:[1,0,0]
	v_pk_fma_f32 v[232:233], v[232:233], -0.5, -0.5 op_sel_hi:[1,0,0]
	v_pk_fma_f32 v[234:235], v[234:235], -0.5, -0.5 op_sel_hi:[1,0,0]
	v_pk_mul_f32 v[134:135], v[130:131], v[132:133]
	v_pk_mul_f32 v[146:147], v[142:143], v[144:145]
	v_pk_mul_f32 v[180:181], v[176:177], v[178:179]
	v_pk_mul_f32 v[236:237], v[232:233], v[234:235]
	v_mul_f32_e32 v188, v134, v135
	v_mul_f32_e32 v190, v146, v147
	v_mul_f32_e32 v189, v180, v181
	v_mul_f32_e32 v191, v236, v237
	v_pk_mul_f32 v[192:193], v[188:189], v[190:191]
	v_mul_f32_e32 v162, v192, v193
	v_rcp_f32_e32 v173, v162
	v_pk_add_f32 v[164:165], v[18:19], v[20:21]
	v_pk_add_f32 v[164:165], v[164:165], v[2:3]
	v_pk_add_f32 v[164:165], v[164:165], v[4:5]
	v_pk_add_f32 v[164:165], v[164:165], v[26:27]
	v_pk_add_f32 v[164:165], v[164:165], v[28:29]
	v_pk_add_f32 v[164:165], v[164:165], v[10:11]
	v_pk_add_f32 v[164:165], v[164:165], v[12:13]
	v_pk_mul_f32 v[230:231], v[172:173], v[192:193] op_sel:[1,1] op_sel_hi:[1,0]
	v_pk_mul_f32 v[192:193], v[230:231], v[190:191]
	v_pk_mul_f32 v[190:191], v[230:231], v[188:189]
	v_pk_mul_f32 v[136:137], v[192:193], v[134:135] op_sel:[0,1] op_sel_hi:[0,0]
	v_pk_mul_f32 v[148:149], v[190:191], v[146:147] op_sel:[0,1] op_sel_hi:[0,0]
	v_pk_mul_f32 v[182:183], v[192:193], v[180:181] op_sel:[1,1] op_sel_hi:[1,0]
	v_pk_mul_f32 v[238:239], v[190:191], v[236:237] op_sel:[1,1] op_sel_hi:[1,0]
	v_pk_fma_f32 v[138:139], v[136:137], v[132:133], 1.0 op_sel_hi:[1,1,0]
	v_pk_fma_f32 v[140:141], v[136:137], v[130:131], 1.0 op_sel_hi:[1,1,0]
	v_pk_fma_f32 v[150:151], v[148:149], v[144:145], 1.0 op_sel_hi:[1,1,0]
	v_pk_fma_f32 v[152:153], v[148:149], v[142:143], 1.0 op_sel_hi:[1,1,0]
	v_pk_fma_f32 v[184:185], v[182:183], v[178:179], 1.0 op_sel_hi:[1,1,0]
	v_pk_fma_f32 v[186:187], v[182:183], v[176:177], 1.0 op_sel_hi:[1,1,0]
	v_pk_fma_f32 v[240:241], v[238:239], v[234:235], 1.0 op_sel_hi:[1,1,0]
	v_pk_fma_f32 v[242:243], v[238:239], v[232:233], 1.0 op_sel_hi:[1,1,0]
	v_cvt_pk_bf16_f32 v154, v138, v139
	v_cvt_pk_bf16_f32 v155, v140, v141
	v_cvt_pk_bf16_f32 v156, v150, v151
	v_cvt_pk_bf16_f32 v157, v152, v153
	v_cvt_pk_bf16_f32 v158, v184, v185
	v_cvt_pk_bf16_f32 v159, v186, v187
	v_cvt_pk_bf16_f32 v160, v240, v241
	v_cvt_pk_bf16_f32 v161, v242, v243
	ds_read_b128 v[18:21], v172
	ds_read_b128 v[2:5], v172 offset:64
	ds_read_b128 v[26:29], v172 offset:128
	ds_read_b128 v[10:13], v172 offset:192
	v_permlane16_swap_b32_e32 v154, v156
	v_permlane16_swap_b32_e32 v155, v157
	global_store_dwordx4 v228, v[154:157], s[60:61] offset:2048 nt
	v_permlane16_swap_b32_e32 v158, v160
	v_permlane16_swap_b32_e32 v159, v161
	global_store_dwordx4 v228, v[158:161], s[60:61] offset:2176 nt
	v_exp_f32_e32 v130, v22
	v_exp_f32_e32 v131, v23
	v_exp_f32_e32 v132, v24
	v_exp_f32_e32 v133, v25
	v_exp_f32_e32 v142, v6
	v_exp_f32_e32 v143, v7
	v_exp_f32_e32 v144, v8
	v_exp_f32_e32 v145, v9
	v_exp_f32_e32 v176, v30
	v_exp_f32_e32 v177, v31
	v_exp_f32_e32 v178, v32
	v_exp_f32_e32 v179, v33
	v_exp_f32_e32 v232, v14
	v_exp_f32_e32 v233, v15
	v_exp_f32_e32 v234, v16
	v_exp_f32_e32 v235, v17
	v_pk_fma_f32 v[130:131], v[130:131], -0.5, -0.5 op_sel_hi:[1,0,0]
	v_pk_fma_f32 v[132:133], v[132:133], -0.5, -0.5 op_sel_hi:[1,0,0]
	v_pk_fma_f32 v[142:143], v[142:143], -0.5, -0.5 op_sel_hi:[1,0,0]
	v_pk_fma_f32 v[144:145], v[144:145], -0.5, -0.5 op_sel_hi:[1,0,0]
	v_pk_fma_f32 v[176:177], v[176:177], -0.5, -0.5 op_sel_hi:[1,0,0]
	v_pk_fma_f32 v[178:179], v[178:179], -0.5, -0.5 op_sel_hi:[1,0,0]
	v_pk_fma_f32 v[232:233], v[232:233], -0.5, -0.5 op_sel_hi:[1,0,0]
	v_pk_fma_f32 v[234:235], v[234:235], -0.5, -0.5 op_sel_hi:[1,0,0]
	v_pk_mul_f32 v[134:135], v[130:131], v[132:133]
	v_pk_mul_f32 v[146:147], v[142:143], v[144:145]
	v_pk_mul_f32 v[180:181], v[176:177], v[178:179]
	v_pk_mul_f32 v[236:237], v[232:233], v[234:235]
	v_mul_f32_e32 v188, v134, v135
	v_mul_f32_e32 v190, v146, v147
	v_mul_f32_e32 v189, v180, v181
	v_mul_f32_e32 v191, v236, v237
	v_pk_mul_f32 v[192:193], v[188:189], v[190:191]
	v_mul_f32_e32 v174, v192, v193
	v_rcp_f32_e32 v173, v174
	v_pk_add_f32 v[164:165], v[164:165], v[22:23]
	v_pk_add_f32 v[164:165], v[164:165], v[24:25]
	v_pk_add_f32 v[164:165], v[164:165], v[6:7]
	v_pk_add_f32 v[164:165], v[164:165], v[8:9]
	v_pk_add_f32 v[164:165], v[164:165], v[30:31]
	v_pk_add_f32 v[164:165], v[164:165], v[32:33]
	v_pk_add_f32 v[164:165], v[164:165], v[14:15]
	v_pk_add_f32 v[164:165], v[164:165], v[16:17]
	v_pk_mul_f32 v[230:231], v[172:173], v[192:193] op_sel:[1,1] op_sel_hi:[1,0]
	v_pk_mul_f32 v[192:193], v[230:231], v[190:191]
	v_pk_mul_f32 v[190:191], v[230:231], v[188:189]
	v_pk_mul_f32 v[136:137], v[192:193], v[134:135] op_sel:[0,1] op_sel_hi:[0,0]
	v_pk_mul_f32 v[148:149], v[190:191], v[146:147] op_sel:[0,1] op_sel_hi:[0,0]
	v_pk_mul_f32 v[182:183], v[192:193], v[180:181] op_sel:[1,1] op_sel_hi:[1,0]
	v_pk_mul_f32 v[238:239], v[190:191], v[236:237] op_sel:[1,1] op_sel_hi:[1,0]
	v_pk_fma_f32 v[138:139], v[136:137], v[132:133], 1.0 op_sel_hi:[1,1,0]
	v_pk_fma_f32 v[140:141], v[136:137], v[130:131], 1.0 op_sel_hi:[1,1,0]
	v_pk_fma_f32 v[150:151], v[148:149], v[144:145], 1.0 op_sel_hi:[1,1,0]
	v_pk_fma_f32 v[152:153], v[148:149], v[142:143], 1.0 op_sel_hi:[1,1,0]
	v_pk_fma_f32 v[184:185], v[182:183], v[178:179], 1.0 op_sel_hi:[1,1,0]
	v_pk_fma_f32 v[186:187], v[182:183], v[176:177], 1.0 op_sel_hi:[1,1,0]
	v_pk_fma_f32 v[240:241], v[238:239], v[234:235], 1.0 op_sel_hi:[1,1,0]
	v_pk_fma_f32 v[242:243], v[238:239], v[232:233], 1.0 op_sel_hi:[1,1,0]
	v_cvt_pk_bf16_f32 v154, v138, v139
	v_cvt_pk_bf16_f32 v155, v140, v141
	v_cvt_pk_bf16_f32 v156, v150, v151
	v_cvt_pk_bf16_f32 v157, v152, v153
	v_cvt_pk_bf16_f32 v158, v184, v185
	v_cvt_pk_bf16_f32 v159, v186, v187
	v_cvt_pk_bf16_f32 v160, v240, v241
	v_cvt_pk_bf16_f32 v161, v242, v243
	ds_read_b128 v[22:25], v172 offset:512
	ds_read_b128 v[6:9], v172 offset:576
	ds_read_b128 v[30:33], v172 offset:640
	ds_read_b128 v[14:17], v172 offset:704
	v_permlane16_swap_b32_e32 v154, v156
	v_permlane16_swap_b32_e32 v155, v157
	global_store_dwordx4 v228, v[154:157], s[64:65] offset:2048 nt
	v_permlane16_swap_b32_e32 v158, v160
	v_permlane16_swap_b32_e32 v159, v161
	global_store_dwordx4 v228, v[158:161], s[64:65] offset:2176 nt
	v_mul_f32_e32 v166, v162, v174
	v_log_f32_e32 v166, v166
	v_add_f32_e32 v168, v164, v165
	v_mul_f32_e32 v168, 0xbeb17218, v168
	v_fmac_f32_e32 v168, 0x3f317218, v166
	v_mov_b32_e32 v169, v168
	s_nop 1
	v_permlane16_swap_b32_e32 v168, v169
	v_add_f32_e32 v168, v168, v169
	v_mov_b32_e32 v169, v168
	s_nop 1
	v_permlane32_swap_b32_e32 v168, v169
	v_add_f32_e32 v168, v168, v169
	s_mov_b64 exec, s[0:1]
	global_store_dword v229, v168, s[66:67] offset:576
	s_mov_b64 exec, -1
	s_cmp_eq_u32 s40, 8
	s_cbranch_scc1 .Lg1_last_tile
	s_mov_b32 s2, s40
	s_add_i32 s40, s40, 1
	s_mov_b32 s41, s12
	s_lshl_b32 s12, s40, 5
	s_cmp_eq_u32 s2, 7
	s_cselect_b64 s[2:3], -1, 0
	s_and_b64 s[16:17], s[2:3], exec
	s_cselect_b32 s12, 0xe0, s12
	s_add_i32 s16, s12, s18
	s_lshr_b32 s12, s16, 4
	s_and_b32 s12, s12, 0xfffff8
	s_lshl_b32 s16, s16, 5
	s_mov_b32 s42, s35
	s_or_b32 s12, s12, s19
	s_and_b32 s35, s16, 0xf00
	s_lshl_b32 s16, s40, 10
	s_lshl_b32 s12, s12, 8
	s_and_b32 s43, s16, 0x400
	s_or_b64 s[2:3], vcc, s[2:3]
	s_lshl_b32 s44, s41, 7
	v_lshl_add_u64 v[202:203], s[12:13], 2, v[196:197]
	s_mov_b32 s45, 0x404000
	s_xor_b64 s[2:3], s[2:3], -1
	v_add_u32_e32 v194, s43, v208
	s_mov_b32 s46, 0
	s_bitcmp1_b32 s20, 12
	s_cbranch_scc0 .Lg1_noY
	s_barrier
